# adds: group-B bias table fill with 4 loads in flight, group-A prologue wait leaves tile DMAs in flight, counted vmcnt waits per job in the P2 conversion loop
# speedup vs baseline: 1.0127x; 1.0065x over previous
.LBB0_434:
	s_add_i32 vcc_lo, s15, 11
	s_cmp_eq_u32 vcc_lo, s5
	s_cbranch_scc1 .Lcv_a_first
	s_add_i32 vcc_lo, s15, -4
	s_cmp_eq_u32 vcc_lo, s5
	s_cbranch_scc1 .Lcv_a_last
	s_waitcnt vmcnt(22)
	s_branch .Lcv_a_go
.Lcv_a_first:
	s_waitcnt vmcnt(16)
	s_branch .Lcv_a_go
.Lcv_a_last:
	s_waitcnt vmcnt(6)
.Lcv_a_go:
	v_mul_f32_e32 v98, 0x43000000, v2
	v_mul_f32_e32 v135, 0x43000000, v6
	v_med3_f32 v98, v98, s3, v122
	v_med3_f32 v135, v135, s3, v122
	v_mov_b32_e32 v137, 0
	v_cvt_pk_fp8_f32 v137, v98, v135
	v_mul_f32_e32 v136, 0x43000000, v10
	v_mul_f32_e32 v135, 0x43000000, v14
	s_and_b32 s10, s4, 0x4000
	v_med3_f32 v98, v136, s3, v122
	v_med3_f32 v135, v135, s3, v122
	v_cvt_pk_fp8_f32 v137, v98, v135 op_sel:[0,0,1]
	v_or_b32_e32 v98, s10, v101
	v_add_u32_e32 v135, v98, v103
	v_add_u32_e32 v144, v135, v107
	v_mul_f32_e32 v135, 0x43000000, v3
	v_mul_f32_e32 v136, 0x43000000, v7
	v_med3_f32 v135, v135, s3, v122
	v_med3_f32 v136, v136, s3, v122
	v_mov_b32_e32 v138, 0
	v_cvt_pk_fp8_f32 v138, v135, v136
	ds_write_b32 v144, v137
	v_mul_f32_e32 v137, 0x43000000, v11
	v_mul_f32_e32 v136, 0x43000000, v15
	v_med3_f32 v135, v137, s3, v122
	v_med3_f32 v136, v136, s3, v122
	v_cvt_pk_fp8_f32 v138, v135, v136 op_sel:[0,0,1]
	v_add_u32_e32 v135, v98, v125
	v_add_u32_e32 v143, v135, v107
	v_mul_f32_e32 v135, 0x43000000, v4
	v_mul_f32_e32 v136, 0x43000000, v8
	v_med3_f32 v135, v135, s3, v122
	v_med3_f32 v136, v136, s3, v122
	v_mov_b32_e32 v139, 0
	v_cvt_pk_fp8_f32 v139, v135, v136
	v_mul_f32_e32 v137, 0x43000000, v12
	v_mul_f32_e32 v136, 0x43000000, v16
	v_med3_f32 v135, v137, s3, v122
	v_med3_f32 v136, v136, s3, v122
	v_cvt_pk_fp8_f32 v139, v135, v136 op_sel:[0,0,1]
	v_add_u32_e32 v135, v98, v126
	v_add_u32_e32 v142, v135, v107
	v_mul_f32_e32 v135, 0x43000000, v5
	v_mul_f32_e32 v136, 0x43000000, v9
	ds_write_b32 v143, v138 offset:256
	v_med3_f32 v135, v135, s3, v122
	v_med3_f32 v136, v136, s3, v122
	v_mov_b32_e32 v138, 0
	v_cvt_pk_fp8_f32 v138, v135, v136
	v_mul_f32_e32 v137, 0x43000000, v13
	v_mul_f32_e32 v136, 0x43000000, v17
	v_med3_f32 v135, v137, s3, v122
	v_med3_f32 v136, v136, s3, v122
	v_cvt_pk_fp8_f32 v138, v135, v136 op_sel:[0,0,1]
	v_add_u32_e32 v135, v98, v127
	v_add_u32_e32 v141, v135, v107
	v_mul_f32_e32 v135, 0x43000000, v18
	v_mul_f32_e32 v136, 0x43000000, v22
	ds_write_b32 v142, v139 offset:512
	v_med3_f32 v135, v135, s3, v122
	v_med3_f32 v136, v136, s3, v122
	v_mov_b32_e32 v139, 0
	v_cvt_pk_fp8_f32 v139, v135, v136
	v_mul_f32_e32 v137, 0x43000000, v34
	v_mul_f32_e32 v136, 0x43000000, v42
	v_med3_f32 v135, v137, s3, v122
	v_med3_f32 v136, v136, s3, v122
	v_cvt_pk_fp8_f32 v139, v135, v136 op_sel:[0,0,1]
	v_add_u32_e32 v135, v98, v128
	v_add_u32_e32 v140, v135, v107
	v_mul_f32_e32 v135, 0x43000000, v19
	v_mul_f32_e32 v136, 0x43000000, v23
	ds_write_b32 v141, v138 offset:768
	v_med3_f32 v135, v135, s3, v122
	v_med3_f32 v136, v136, s3, v122
	v_mov_b32_e32 v138, 0
	v_cvt_pk_fp8_f32 v138, v135, v136
	v_mul_f32_e32 v137, 0x43000000, v35
	v_mul_f32_e32 v136, 0x43000000, v43
	v_med3_f32 v135, v137, s3, v122
	v_med3_f32 v136, v136, s3, v122
	v_cvt_pk_fp8_f32 v138, v135, v136 op_sel:[0,0,1]
	v_add_u32_e32 v135, v98, v129
	ds_write_b32 v140, v139
	v_add_u32_e32 v139, v135, v107
	v_mul_f32_e32 v135, 0x43000000, v20
	v_mul_f32_e32 v136, 0x43000000, v24
	v_med3_f32 v135, v135, s3, v122
	v_med3_f32 v136, v136, s3, v122
	v_mov_b32_e32 v145, 0
	v_cvt_pk_fp8_f32 v145, v135, v136
	v_mul_f32_e32 v137, 0x43000000, v36
	v_mul_f32_e32 v136, 0x43000000, v44
	v_med3_f32 v135, v137, s3, v122
	v_med3_f32 v136, v136, s3, v122
	v_cvt_pk_fp8_f32 v145, v135, v136 op_sel:[0,0,1]
	v_add_u32_e32 v135, v98, v130
	ds_write_b32 v139, v138 offset:256
	v_add_u32_e32 v138, v135, v107
	v_mul_f32_e32 v135, 0x43000000, v21
	v_mul_f32_e32 v136, 0x43000000, v25
	ds_write_b32 v138, v145 offset:512
	v_med3_f32 v135, v135, s3, v122
	v_med3_f32 v136, v136, s3, v122
	v_mov_b32_e32 v145, 0
	v_cvt_pk_fp8_f32 v145, v135, v136
	v_mul_f32_e32 v137, 0x43000000, v37
	v_mul_f32_e32 v136, 0x43000000, v45
	v_med3_f32 v135, v137, s3, v122
	v_med3_f32 v136, v136, s3, v122
	v_cvt_pk_fp8_f32 v145, v135, v136 op_sel:[0,0,1]
	v_add_u32_e32 v98, v98, v131
	s_add_i32 s17, s15, -2
	v_add_u32_e32 v135, v98, v107
	s_cmp_ge_i32 s17, s5
	ds_write_b32 v135, v145 offset:768
	s_cbranch_scc1 .LBB0_436
	s_add_i32 s11, s16, 0x300
	s_ashr_i32 s6, s17, 5
	s_and_b32 s11, s11, 0x300
	s_ashr_i32 s7, s6, 31
	v_add_u32_e32 v4, s11, v102
	s_lshl_b64 s[18:19], s[6:7], 20
	v_ashrrev_i32_e32 v5, 31, v4
	v_lshl_add_u64 v[2:3], v[104:105], 0, s[18:19]
	v_lshlrev_b64 v[4:5], 10, v[4:5]
	s_lshl_b32 s18, s17, 5
	v_lshl_add_u64 v[2:3], v[2:3], 0, v[4:5]
	s_and_b32 s76, s18, 0x200
	v_lshl_add_u64 v[2:3], v[2:3], 0, s[76:77]
	s_and_b32 s76, s18, 0x180
	v_lshl_add_u64 v[2:3], v[2:3], 0, s[76:77]
	v_lshlrev_b32_e32 v98, 2, v106
	v_lshl_add_u64 v[2:3], v[2:3], 0, v[98:99]
	v_lshlrev_b32_e32 v98, 2, v100
	v_lshl_add_u64 v[18:19], v[2:3], 0, v[98:99]
	v_add_co_u32_e32 v42, vcc, s84, v18
	global_load_dwordx4 v[2:5], v[18:19], off
	global_load_dwordx4 v[6:9], v[18:19], off offset:1024
	global_load_dwordx4 v[10:13], v[18:19], off offset:2048
	global_load_dwordx4 v[14:17], v[18:19], off offset:3072
	v_addc_co_u32_e32 v43, vcc, 0, v19, vcc
	global_load_dwordx4 v[18:21], v[42:43], off
	global_load_dwordx4 v[22:25], v[42:43], off offset:1024
	global_load_dwordx4 v[34:37], v[42:43], off offset:2048
	s_nop 0
	global_load_dwordx4 v[42:45], v[42:43], off offset:3072
	s_lshl_b64 s[6:7], s[6:7], 19
	s_add_u32 s6, s56, s6
	s_addc_u32 s7, s57, s7
	s_lshl_b32 s18, s17, 14
	s_and_b32 s18, s18, 0x70000
	s_add_u32 s6, s6, s18
	s_addc_u32 s7, s7, 0
	s_add_u32 s6, s6, s11
	s_addc_u32 s7, s7, 0
.LBB0_436:
	v_add_u32_e32 v98, s10, v132
	v_add_u32_e32 v136, v98, v133
	s_waitcnt lgkmcnt(0)
	s_barrier
	ds_read_b128 v[146:149], v136
	v_lshl_add_u64 v[150:151], s[12:13], 0, v[108:109]
	v_lshl_add_u64 v[152:153], v[150:151], 0, v[110:111]
	v_add_u32_e32 v137, v98, v134
	s_add_i32 s10, s15, -4
	s_waitcnt lgkmcnt(0)
	global_store_dwordx4 v[152:153], v[146:149], off
	ds_read_b128 v[146:149], v137
	v_lshl_add_u64 v[150:151], v[150:151], 0, v[112:113]
	s_mov_b64 s[12:13], -1
	s_cmp_ge_i32 s10, s5
	s_waitcnt lgkmcnt(0)
	global_store_dwordx4 v[150:151], v[146:149], off
	s_cbranch_scc1 .LBB0_433
	s_add_i32 vcc_lo, s15, 11
	s_cmp_eq_u32 vcc_lo, s5
	s_cbranch_scc1 .Lcv_b_first
	s_waitcnt vmcnt(22)
	s_branch .Lcv_b_go
.Lcv_b_first:
	s_waitcnt vmcnt(18)
.Lcv_b_go:
	v_mul_f32_e32 v98, 0x43000000, v30
	v_mul_f32_e32 v145, 0x43000000, v26
	v_med3_f32 v98, v98, s3, v122
	v_med3_f32 v145, v145, s3, v122
	v_mov_b32_e32 v147, 0
	v_cvt_pk_fp8_f32 v147, v98, v145
	v_mul_f32_e32 v146, 0x43000000, v38
	v_mul_f32_e32 v145, 0x43000000, v46
	v_med3_f32 v98, v146, s3, v122
	v_med3_f32 v145, v145, s3, v122
	v_cvt_pk_fp8_f32 v147, v98, v145 op_sel:[0,0,1]
	v_mul_f32_e32 v145, 0x43000000, v31
	v_mul_f32_e32 v146, 0x43000000, v27
	v_med3_f32 v145, v145, s3, v122
	v_med3_f32 v146, v146, s3, v122
	v_mov_b32_e32 v149, 0
	v_cvt_pk_fp8_f32 v149, v145, v146
	v_mul_f32_e32 v148, 0x43000000, v39
	v_mul_f32_e32 v146, 0x43000000, v47
	s_add_i32 s10, s4, 0x4000
	v_med3_f32 v145, v148, s3, v122
	v_med3_f32 v146, v146, s3, v122
	s_and_b32 s12, s10, 0x4000
	v_cvt_pk_fp8_f32 v149, v145, v146 op_sel:[0,0,1]
	v_or_b32_e32 v98, s12, v101
	v_add3_u32 v145, v98, v103, v107
	ds_write_b32 v145, v147
	v_add3_u32 v145, v98, v125, v107
	ds_write_b32 v145, v149 offset:256
	v_mul_f32_e32 v145, 0x43000000, v32
	v_mul_f32_e32 v146, 0x43000000, v28
	v_med3_f32 v145, v145, s3, v122
	v_med3_f32 v146, v146, s3, v122
	v_mov_b32_e32 v148, 0
	v_cvt_pk_fp8_f32 v148, v145, v146
	v_mul_f32_e32 v147, 0x43000000, v40
	v_mul_f32_e32 v146, 0x43000000, v48
	v_med3_f32 v145, v147, s3, v122
	v_med3_f32 v146, v146, s3, v122
	v_cvt_pk_fp8_f32 v148, v145, v146 op_sel:[0,0,1]
	v_mul_f32_e32 v145, 0x43000000, v33
	v_mul_f32_e32 v146, 0x43000000, v29
	v_med3_f32 v145, v145, s3, v122
	v_med3_f32 v146, v146, s3, v122
	v_mov_b32_e32 v149, 0
	v_cvt_pk_fp8_f32 v149, v145, v146
	v_mul_f32_e32 v147, 0x43000000, v41
	v_mul_f32_e32 v146, 0x43000000, v49
	v_med3_f32 v145, v147, s3, v122
	v_med3_f32 v146, v146, s3, v122
	v_cvt_pk_fp8_f32 v149, v145, v146 op_sel:[0,0,1]
	v_add3_u32 v145, v98, v126, v107
	ds_write_b32 v145, v148 offset:512
	v_add3_u32 v145, v98, v127, v107
	ds_write_b32 v145, v149 offset:768
	v_mul_f32_e32 v145, 0x43000000, v50
	v_mul_f32_e32 v146, 0x43000000, v54
	v_med3_f32 v145, v145, s3, v122
	v_med3_f32 v146, v146, s3, v122
	v_mov_b32_e32 v148, 0
	v_cvt_pk_fp8_f32 v148, v145, v146
	v_mul_f32_e32 v147, 0x43000000, v66
	v_mul_f32_e32 v146, 0x43000000, v74
	v_med3_f32 v145, v147, s3, v122
	v_med3_f32 v146, v146, s3, v122
	v_cvt_pk_fp8_f32 v148, v145, v146 op_sel:[0,0,1]
	v_mul_f32_e32 v145, 0x43000000, v51
	v_mul_f32_e32 v146, 0x43000000, v55
	v_med3_f32 v145, v145, s3, v122
	v_med3_f32 v146, v146, s3, v122
	v_mov_b32_e32 v149, 0
	v_cvt_pk_fp8_f32 v149, v145, v146
	v_mul_f32_e32 v147, 0x43000000, v67
	v_mul_f32_e32 v146, 0x43000000, v75
	v_med3_f32 v145, v147, s3, v122
	v_med3_f32 v146, v146, s3, v122
	v_cvt_pk_fp8_f32 v149, v145, v146 op_sel:[0,0,1]
	v_add3_u32 v145, v98, v128, v107
	ds_write_b32 v145, v148
	v_add3_u32 v145, v98, v129, v107
	ds_write_b32 v145, v149 offset:256
	v_mul_f32_e32 v145, 0x43000000, v52
	v_mul_f32_e32 v146, 0x43000000, v56
	v_med3_f32 v145, v145, s3, v122
	v_med3_f32 v146, v146, s3, v122
	v_mov_b32_e32 v148, 0
	v_cvt_pk_fp8_f32 v148, v145, v146
	v_mul_f32_e32 v147, 0x43000000, v68
	v_mul_f32_e32 v146, 0x43000000, v76
	v_med3_f32 v145, v147, s3, v122
	v_med3_f32 v146, v146, s3, v122
	v_cvt_pk_fp8_f32 v148, v145, v146 op_sel:[0,0,1]
	v_mul_f32_e32 v145, 0x43000000, v53
	v_mul_f32_e32 v146, 0x43000000, v57
	v_med3_f32 v145, v145, s3, v122
	v_med3_f32 v146, v146, s3, v122
	v_mov_b32_e32 v149, 0
	v_cvt_pk_fp8_f32 v149, v145, v146
	v_mul_f32_e32 v147, 0x43000000, v69
	v_mul_f32_e32 v146, 0x43000000, v77
	v_med3_f32 v145, v147, s3, v122
	v_med3_f32 v146, v146, s3, v122
	v_cvt_pk_fp8_f32 v149, v145, v146 op_sel:[0,0,1]
	s_add_i32 s13, s15, -1
	v_add3_u32 v145, v98, v130, v107
	v_add3_u32 v98, v98, v131, v107
	s_cmp_ge_i32 s13, s5
	s_mov_b64 s[10:11], s[8:9]
	ds_write_b32 v145, v148 offset:512
	ds_write_b32 v98, v149 offset:768
	s_cbranch_scc1 .LBB0_439
	s_ashr_i32 s10, s13, 5
	s_ashr_i32 s11, s10, 31
	s_lshl_b64 s[18:19], s[10:11], 20
	v_lshl_add_u64 v[26:27], v[104:105], 0, s[18:19]
	s_and_b32 s18, s16, 0x300
	v_add_u32_e32 v28, s18, v102
	v_ashrrev_i32_e32 v29, 31, v28
	v_lshlrev_b64 v[28:29], 10, v[28:29]
	s_lshl_b32 s19, s13, 5
	v_lshl_add_u64 v[26:27], v[26:27], 0, v[28:29]
	s_and_b32 s76, s19, 0x200
	v_lshl_add_u64 v[26:27], v[26:27], 0, s[76:77]
	s_and_b32 s76, s19, 0x180
	v_lshl_add_u64 v[26:27], v[26:27], 0, s[76:77]
	v_lshlrev_b32_e32 v98, 2, v106
	v_lshl_add_u64 v[26:27], v[26:27], 0, v[98:99]
	v_lshlrev_b32_e32 v98, 2, v100
	v_lshl_add_u64 v[50:51], v[26:27], 0, v[98:99]
	v_add_co_u32_e32 v74, vcc, s84, v50
	global_load_dwordx4 v[30:33], v[50:51], off
	global_load_dwordx4 v[26:29], v[50:51], off offset:1024
	global_load_dwordx4 v[38:41], v[50:51], off offset:2048
	global_load_dwordx4 v[46:49], v[50:51], off offset:3072
	v_addc_co_u32_e32 v75, vcc, 0, v51, vcc
	global_load_dwordx4 v[50:53], v[74:75], off
	global_load_dwordx4 v[54:57], v[74:75], off offset:1024
	global_load_dwordx4 v[66:69], v[74:75], off offset:2048
	s_nop 0
	global_load_dwordx4 v[74:77], v[74:75], off offset:3072
	s_lshl_b64 s[10:11], s[10:11], 19
	s_add_u32 s10, s56, s10
	s_addc_u32 s11, s57, s11
	s_lshl_b32 s13, s13, 14
	s_and_b32 s13, s13, 0x70000
	s_add_u32 s10, s10, s13
	s_addc_u32 s11, s11, 0
	s_add_u32 s10, s10, s18
	s_addc_u32 s11, s11, 0
; __device__ void conv_jobs_deep(const Params& p, unsigned char* smem, int j0, int j1) {
;     ...
;     if (j0 >= j1) return;
;     ConvJob ja = conv_job_decode(p, j0, tid), jb = ja, jc = ja;
;     CV_LOAD(ja, a0, a1, a2, a3, a4, a5, a6, a7);
;     if (j0 + 1 < j1) { jb = conv_job_decode(p, j0 + 1, tid); CV_LOAD(jb, b0, b1, b2, b3, b4, b5, b6, b7); }
;     if (j0 + 2 < j1) { jc = conv_job_decode(p, j0 + 2, tid); CV_LOAD(jc, c0, c1, c2, c3, c4, c5, c6, c7); }
;     for (int j = j0; j < j1; j += 3) {
;         CD_PROC(ja, j, a0, a1, a2, a3, a4, a5, a6, a7);
;         if (j + 1 >= j1) break;
;         CD_PROC(jb, j + 1, b0, b1, b2, b3, b4, b5, b6, b7);
;         if (j + 2 >= j1) break;
;         CD_PROC(jc, j + 2, c0, c1, c2, c3, c4, c5, c6, c7);
.LBB0_439:
	v_add_u32_e32 v98, s12, v132
	v_add_u32_e32 v145, v98, v133
	s_waitcnt lgkmcnt(0)
	s_barrier
	ds_read_b128 v[146:149], v145
	v_lshl_add_u64 v[150:151], s[8:9], 0, v[108:109]
	v_lshl_add_u64 v[152:153], v[150:151], 0, v[110:111]
	v_add_u32_e32 v98, v98, v134
	s_add_i32 s18, s15, -5
	s_waitcnt lgkmcnt(0)
	global_store_dwordx4 v[152:153], v[146:149], off
	ds_read_b128 v[146:149], v98
	v_lshl_add_u64 v[150:151], v[150:151], 0, v[112:113]
	s_mov_b64 s[12:13], -1
	s_cmp_ge_i32 s18, s14
	s_waitcnt lgkmcnt(0)
	global_store_dwordx4 v[150:151], v[146:149], off
	s_cbranch_scc1 .LBB0_433
	s_add_i32 vcc_lo, s15, 11
	s_cmp_eq_u32 vcc_lo, s5
	s_cbranch_scc1 .Lcv_c_first
	s_add_i32 vcc_lo, s15, -1
	s_cmp_eq_u32 vcc_lo, s5
	s_cbranch_scc1 .Lcv_c_last
	s_waitcnt vmcnt(22)
	s_branch .Lcv_c_go
.Lcv_c_first:
	s_waitcnt vmcnt(20)
	s_branch .Lcv_c_go
.Lcv_c_last:
	s_waitcnt vmcnt(14)
.Lcv_c_go:
	v_mul_f32_e32 v98, 0x43000000, v62
	v_mul_f32_e32 v145, 0x43000000, v58
	v_med3_f32 v98, v98, s3, v122
	v_med3_f32 v145, v145, s3, v122
	v_mov_b32_e32 v148, 0
	v_cvt_pk_fp8_f32 v148, v98, v145
	v_mul_f32_e32 v146, 0x43000000, v70
	v_mul_f32_e32 v147, 0x43000000, v78
	v_med3_f32 v146, v146, s3, v122
	v_med3_f32 v147, v147, s3, v122
	v_cvt_pk_fp8_f32 v148, v146, v147 op_sel:[0,0,1]
	v_mul_f32_e32 v98, 0x43000000, v63
	v_med3_f32 v98, v98, s3, v122
	v_mov_b32_e32 v147, 0
	ds_write_b32 v144, v148
	v_mul_f32_e32 v144, 0x43000000, v59
	v_med3_f32 v144, v144, s3, v122
	v_cvt_pk_fp8_f32 v147, v98, v144
	v_mul_f32_e32 v145, 0x43000000, v71
	v_mul_f32_e32 v146, 0x43000000, v79
	v_med3_f32 v145, v145, s3, v122
	v_med3_f32 v146, v146, s3, v122
	v_cvt_pk_fp8_f32 v147, v145, v146 op_sel:[0,0,1]
	v_mul_f32_e32 v98, 0x43000000, v64
	v_med3_f32 v98, v98, s3, v122
	v_mov_b32_e32 v146, 0
	ds_write_b32 v143, v147 offset:256
	v_mul_f32_e32 v143, 0x43000000, v60
	v_med3_f32 v143, v143, s3, v122
	v_cvt_pk_fp8_f32 v146, v98, v143
	v_mul_f32_e32 v144, 0x43000000, v72
	v_mul_f32_e32 v145, 0x43000000, v80
	v_med3_f32 v144, v144, s3, v122
	v_med3_f32 v145, v145, s3, v122
	v_cvt_pk_fp8_f32 v146, v144, v145 op_sel:[0,0,1]
	v_mul_f32_e32 v98, 0x43000000, v65
	v_med3_f32 v98, v98, s3, v122
	v_mov_b32_e32 v145, 0
	ds_write_b32 v142, v146 offset:512
	v_mul_f32_e32 v142, 0x43000000, v61
	v_med3_f32 v142, v142, s3, v122
	v_cvt_pk_fp8_f32 v145, v98, v142
	v_mul_f32_e32 v143, 0x43000000, v73
	v_mul_f32_e32 v144, 0x43000000, v81
	v_med3_f32 v143, v143, s3, v122
	v_med3_f32 v144, v144, s3, v122
	v_cvt_pk_fp8_f32 v145, v143, v144 op_sel:[0,0,1]
	v_mul_f32_e32 v98, 0x43000000, v82
	v_med3_f32 v98, v98, s3, v122
	v_mov_b32_e32 v144, 0
	ds_write_b32 v141, v145 offset:768
	v_mul_f32_e32 v141, 0x43000000, v86
	v_med3_f32 v141, v141, s3, v122
	v_cvt_pk_fp8_f32 v144, v98, v141
	v_mul_f32_e32 v142, 0x43000000, v90
	v_mul_f32_e32 v143, 0x43000000, v94
	v_med3_f32 v142, v142, s3, v122
	v_med3_f32 v143, v143, s3, v122
	v_cvt_pk_fp8_f32 v144, v142, v143 op_sel:[0,0,1]
	v_mul_f32_e32 v98, 0x43000000, v83
	v_med3_f32 v98, v98, s3, v122
	v_mov_b32_e32 v143, 0
	ds_write_b32 v140, v144
	v_mul_f32_e32 v140, 0x43000000, v87
	v_med3_f32 v140, v140, s3, v122
	v_cvt_pk_fp8_f32 v143, v98, v140
	v_mul_f32_e32 v141, 0x43000000, v91
	v_mul_f32_e32 v142, 0x43000000, v95
	v_med3_f32 v141, v141, s3, v122
	v_med3_f32 v142, v142, s3, v122
	v_cvt_pk_fp8_f32 v143, v141, v142 op_sel:[0,0,1]
	v_mul_f32_e32 v98, 0x43000000, v84
	v_med3_f32 v98, v98, s3, v122
	v_mov_b32_e32 v142, 0
	ds_write_b32 v139, v143 offset:256
	v_mul_f32_e32 v139, 0x43000000, v88
	v_med3_f32 v139, v139, s3, v122
	v_cvt_pk_fp8_f32 v142, v98, v139
	v_mul_f32_e32 v140, 0x43000000, v92
	v_mul_f32_e32 v141, 0x43000000, v96
	v_med3_f32 v140, v140, s3, v122
	v_med3_f32 v141, v141, s3, v122
	v_cvt_pk_fp8_f32 v142, v140, v141 op_sel:[0,0,1]
	v_mul_f32_e32 v98, 0x43000000, v85
	v_med3_f32 v98, v98, s3, v122
	v_mov_b32_e32 v141, 0
	ds_write_b32 v138, v142 offset:512
	v_mul_f32_e32 v138, 0x43000000, v89
	v_med3_f32 v138, v138, s3, v122
	v_cvt_pk_fp8_f32 v141, v98, v138
	v_mul_f32_e32 v139, 0x43000000, v93
	v_mul_f32_e32 v140, 0x43000000, v97
	v_med3_f32 v139, v139, s3, v122
	v_med3_f32 v140, v140, s3, v122
	v_cvt_pk_fp8_f32 v141, v139, v140 op_sel:[0,0,1]
	s_cmp_ge_i32 s15, s5
	s_mov_b64 s[8:9], s[0:1]
	ds_write_b32 v135, v141 offset:768
	s_cbranch_scc1 .LBB0_432
	s_ashr_i32 s8, s15, 5
	s_ashr_i32 s9, s8, 31
	s_lshl_b64 s[12:13], s[8:9], 20
	v_lshl_add_u64 v[58:59], v[104:105], 0, s[12:13]
	s_add_i32 s12, s16, 0x500
	s_and_b32 s12, s12, 0x300
	v_add_u32_e32 v60, s12, v102
	v_ashrrev_i32_e32 v61, 31, v60
	v_lshlrev_b64 v[60:61], 10, v[60:61]
	s_lshl_b32 s13, s15, 5
	v_lshl_add_u64 v[58:59], v[58:59], 0, v[60:61]
	s_and_b32 s76, s13, 0x200
	v_lshl_add_u64 v[58:59], v[58:59], 0, s[76:77]
	s_and_b32 s76, s13, 0x180
	v_lshl_add_u64 v[58:59], v[58:59], 0, s[76:77]
	v_lshlrev_b32_e32 v98, 2, v106
	v_lshl_add_u64 v[58:59], v[58:59], 0, v[98:99]
	v_lshlrev_b32_e32 v98, 2, v100
	v_lshl_add_u64 v[82:83], v[58:59], 0, v[98:99]
	v_add_co_u32_e32 v94, vcc, s84, v82
	global_load_dwordx4 v[62:65], v[82:83], off
	global_load_dwordx4 v[58:61], v[82:83], off offset:1024
	global_load_dwordx4 v[70:73], v[82:83], off offset:2048
	global_load_dwordx4 v[78:81], v[82:83], off offset:3072
	v_addc_co_u32_e32 v95, vcc, 0, v83, vcc
	global_load_dwordx4 v[82:85], v[94:95], off
	global_load_dwordx4 v[86:89], v[94:95], off offset:1024
	global_load_dwordx4 v[90:93], v[94:95], off offset:2048
	s_nop 0
	global_load_dwordx4 v[94:97], v[94:95], off offset:3072
	s_lshl_b64 s[8:9], s[8:9], 19
	s_add_u32 s8, s56, s8
	s_addc_u32 s9, s57, s9
	s_lshl_b32 s13, s15, 14
	s_and_b32 s13, s13, 0x70000
	s_add_u32 s8, s8, s13
	s_addc_u32 s9, s9, 0
	s_add_u32 s8, s8, s12
	s_addc_u32 s9, s9, 0
	s_branch .LBB0_432
